# RGATE phase: per-XCD staggered start so epilogue HBM bursts interleave with other XCDs' K-loops
# baseline (speedup 1.0000x reference)
; #define LAS __attribute__((address_space(3)))
; #define GET_TID() int tid; asm volatile("v_mbcnt_lo_u32_b32 %0, -1, 0\n\tv_mbcnt_hi_u32_b32 %0, -1, %0" : "=v"(tid)); const int lane = tid; tid += wave0 * 64; (void)lane;
; __global__ void __launch_bounds__(NTHREADS, 2) mk_fwd(Args args) {
;     ...
;         } else {
;             GET_TID()
;             pg8::Gemm g{P_XH, P_WA + (size_t)(2 * D + DV) * D, M, 2 * DV, D, 0}; pg8::StaticOrder S; S.init(M, 2 * DV, G, bid);
;             pg8::stage_scales(lds + RING_OFF, S, RS, false, 0, tid);
;             pg8::EpiGate E{P_YC, (const bf16*)out, P_LSE, (const LAS float*)(lds + RING_OFF + pg8::RS_TAB_OFF)};
;             pg8::gemm_phase<pg8::EpiGate, pg8::StaticOrder, true, true>(lds + RING_OFF, g, S, E, tid);
.LBB0_312:
	s_and_b32 s98, s90, 7
	s_cmp_eq_u32 s98, 0
	s_cbranch_scc1 .Lrg_skew_done
.Lrg_skew_loop:
	s_sleep 96
	s_sub_i32 s98, s98, 1
	s_cmp_lg_u32 s98, 0
	s_cbranch_scc1 .Lrg_skew_loop
